# MLA attention: cross-half running-max exchange by v_permlane32_swap instead of ds_bpermute (no LDS round trip on the softmax critical path)
# speedup vs baseline: 1.0180x; 1.0042x over previous
.LBB0_827:
	s_nop 10
	v_max3_f32 v2, v36, v37, v38
	v_max3_f32 v152, v52, v53, v54
	v_max3_f32 v2, v2, v39, v40
	v_max3_f32 v152, v152, v55, v56
	v_max3_f32 v2, v2, v41, v42
	v_max3_f32 v152, v152, v57, v58
	v_max3_f32 v2, v2, v43, v44
	v_max3_f32 v152, v152, v59, v60
	v_max3_f32 v2, v2, v45, v46
	v_max3_f32 v152, v152, v61, v62
	v_max3_f32 v2, v2, v47, v48
	v_max3_f32 v152, v152, v63, v64
	v_max3_f32 v2, v2, v49, v50
	v_max3_f32 v152, v152, v65, v66
	v_max3_f32 v2, v2, v51, v67
	v_max_f32_e32 v2, v2, v152
	v_and_b32_e32 v153, 64, v250
	v_xor_b32_e32 v152, 32, v250
	v_add_u32_e32 v153, 64, v153
	v_cmp_lt_i32_e32 vcc, v152, v153
	s_nop 1
	v_cndmask_b32_e32 v152, v250, v152, vcc
	v_lshlrev_b32_e32 v152, 2, v152
	v_mov_b32_e32 v153, v2
	s_nop 1
	v_permlane32_swap_b32_e32 v2, v153
	s_nop 1
	s_waitcnt lgkmcnt(0)
	v_max3_f32 v2, v151, v2, v153
	v_cmp_gt_f32_e32 vcc, v2, v151
	s_cbranch_vccz .LBB0_829
	v_sub_f32_e32 v151, v151, v2
	v_mul_f32_e32 v151, 0x3e16c740, v151
	v_exp_f32_e32 v154, v151
	s_nop 0
	v_mul_f32_e32 v135, v135, v154
	v_pk_mul_f32 v[34:35], v[34:35], v[154:155] op_sel_hi:[1,0]
	v_pk_mul_f32 v[32:33], v[32:33], v[154:155] op_sel_hi:[1,0]
	v_pk_mul_f32 v[30:31], v[30:31], v[154:155] op_sel_hi:[1,0]
	v_pk_mul_f32 v[28:29], v[28:29], v[154:155] op_sel_hi:[1,0]
	v_pk_mul_f32 v[26:27], v[26:27], v[154:155] op_sel_hi:[1,0]
	v_pk_mul_f32 v[24:25], v[24:25], v[154:155] op_sel_hi:[1,0]
	v_pk_mul_f32 v[22:23], v[22:23], v[154:155] op_sel_hi:[1,0]
	v_pk_mul_f32 v[20:21], v[20:21], v[154:155] op_sel_hi:[1,0]
	v_pk_mul_f32 v[18:19], v[18:19], v[154:155] op_sel_hi:[1,0]
	v_pk_mul_f32 v[16:17], v[16:17], v[154:155] op_sel_hi:[1,0]
	v_pk_mul_f32 v[14:15], v[14:15], v[154:155] op_sel_hi:[1,0]
	v_pk_mul_f32 v[12:13], v[12:13], v[154:155] op_sel_hi:[1,0]
	v_pk_mul_f32 v[10:11], v[10:11], v[154:155] op_sel_hi:[1,0]
	v_pk_mul_f32 v[8:9], v[8:9], v[154:155] op_sel_hi:[1,0]
	v_pk_mul_f32 v[6:7], v[6:7], v[154:155] op_sel_hi:[1,0]
	v_pk_mul_f32 v[4:5], v[4:5], v[154:155] op_sel_hi:[1,0]

.LBB0_843:
	s_nop 10
	v_max3_f32 v69, v36, v37, v38
	v_max3_f32 v68, v52, v53, v54
	v_max3_f32 v69, v69, v39, v40
	v_max3_f32 v68, v68, v55, v56
	v_max3_f32 v69, v69, v41, v42
	v_max3_f32 v68, v68, v57, v58
	v_max3_f32 v69, v69, v43, v44
	v_max3_f32 v68, v68, v59, v60
	v_max3_f32 v69, v69, v45, v46
	v_max3_f32 v68, v68, v61, v62
	v_max3_f32 v69, v69, v47, v48
	v_max3_f32 v68, v68, v63, v64
	v_max3_f32 v69, v69, v49, v50
	v_max3_f32 v68, v68, v65, v66
	v_max3_f32 v69, v69, v51, v67
	v_max_f32_e32 v69, v69, v68
	v_and_b32_e32 v70, 64, v250
	v_xor_b32_e32 v68, 32, v250
	v_add_u32_e32 v70, 64, v70
	v_cmp_lt_i32_e32 vcc, v68, v70
	s_nop 1
	v_cndmask_b32_e32 v68, v250, v68, vcc
	v_lshlrev_b32_e32 v68, 2, v68
	v_mov_b32_e32 v70, v69
	s_nop 1
	v_permlane32_swap_b32_e32 v69, v70
	s_nop 1
	s_waitcnt lgkmcnt(0)
	v_max3_f32 v69, v2, v69, v70
	v_cmp_gt_f32_e32 vcc, v69, v2
	s_cbranch_vccz .LBB0_845
	v_sub_f32_e32 v2, v2, v69
	v_mul_f32_e32 v2, 0x3e16c740, v2
	v_exp_f32_e32 v2, v2
	s_nop 0
	v_mul_f32_e32 v135, v135, v2
	v_pk_mul_f32 v[34:35], v[34:35], v[2:3] op_sel_hi:[1,0]
	v_pk_mul_f32 v[32:33], v[32:33], v[2:3] op_sel_hi:[1,0]
	v_pk_mul_f32 v[30:31], v[30:31], v[2:3] op_sel_hi:[1,0]
	v_pk_mul_f32 v[28:29], v[28:29], v[2:3] op_sel_hi:[1,0]
	v_pk_mul_f32 v[26:27], v[26:27], v[2:3] op_sel_hi:[1,0]
	v_pk_mul_f32 v[24:25], v[24:25], v[2:3] op_sel_hi:[1,0]
	v_pk_mul_f32 v[22:23], v[22:23], v[2:3] op_sel_hi:[1,0]
	v_pk_mul_f32 v[20:21], v[20:21], v[2:3] op_sel_hi:[1,0]
	v_pk_mul_f32 v[18:19], v[18:19], v[2:3] op_sel_hi:[1,0]
	v_pk_mul_f32 v[16:17], v[16:17], v[2:3] op_sel_hi:[1,0]
	v_pk_mul_f32 v[14:15], v[14:15], v[2:3] op_sel_hi:[1,0]
	v_pk_mul_f32 v[12:13], v[12:13], v[2:3] op_sel_hi:[1,0]
	v_pk_mul_f32 v[10:11], v[10:11], v[2:3] op_sel_hi:[1,0]
	v_pk_mul_f32 v[8:9], v[8:9], v[2:3] op_sel_hi:[1,0]
	v_pk_mul_f32 v[6:7], v[6:7], v[2:3] op_sel_hi:[1,0]
	v_pk_mul_f32 v[4:5], v[4:5], v[2:3] op_sel_hi:[1,0]
